# attention forget-bias add: 16 v_pk_add_f32 per step replaced by 32 v_sub_f32 (instruction selection beside MFMAs)
# baseline (speedup 1.0000x reference)
.LBB0_727:
	v_mfma_f32_32x32x16_bf16 v[16:31], v[126:129], v[190:193], v[16:31]
	v_exp_f32_e32 v48, v48
	v_exp_f32_e32 v49, v49
	v_exp_f32_e64 v50, v50
	v_exp_f32_e32 v51, v51
	s_waitcnt lgkmcnt(14)
	v_mfma_f32_32x32x16_bf16 v[0:15], v[126:129], v[186:189], v[0:15]
	v_exp_f32_e32 v52, v52
	v_exp_f32_e32 v53, v53
	v_exp_f32_e32 v54, v54
	v_exp_f32_e32 v55, v55
	v_add_u32_e64 v80, s22, v238
	ds_read_b128 v[134:137], v80
	ds_read_b128 v[130:133], v80 offset:512
	v_mfma_f32_32x32x16_bf16 v[16:31], v[122:125], v[182:185], v[16:31]
	v_exp_f32_e32 v56, v56
	v_exp_f32_e32 v57, v57
	v_exp_f32_e32 v58, v58
	v_exp_f32_e32 v59, v59
	ds_read_b128 v[146:149], v80 offset:2048
	ds_read_b128 v[142:145], v80 offset:2560
	v_mfma_f32_32x32x16_bf16 v[0:15], v[122:125], v[178:181], v[0:15]
	v_exp_f32_e32 v60, v60
	v_exp_f32_e32 v61, v61
	v_exp_f32_e32 v62, v62
	v_exp_f32_e32 v63, v63
	ds_read_b128 v[158:161], v80 offset:4096
	ds_read_b128 v[154:157], v80 offset:4608
	v_mfma_f32_32x32x16_bf16 v[16:31], v[118:121], v[166:169], v[16:31]
	v_exp_f32_e32 v32, v32
	v_exp_f32_e32 v33, v33
	v_exp_f32_e32 v34, v34
	v_exp_f32_e32 v35, v35
	ds_read_b128 v[166:169], v80 offset:6144
	ds_read_b128 v[150:153], v80 offset:6656
	s_waitcnt lgkmcnt(14)
	s_nop 0
	v_mfma_f32_32x32x16_bf16 v[0:15], v[118:121], v[174:177], v[0:15]
	v_exp_f32_e32 v36, v36
	v_exp_f32_e32 v37, v37
	v_exp_f32_e32 v38, v38
	v_exp_f32_e32 v39, v39
	v_mfma_f32_32x32x16_bf16 v[16:31], v[114:117], v[170:173], v[16:31]
	v_exp_f32_e32 v40, v40
	v_exp_f32_e32 v41, v41
	v_exp_f32_e32 v42, v42
	v_exp_f32_e32 v43, v43
	v_mfma_f32_32x32x16_bf16 v[0:15], v[114:117], v[162:165], v[0:15]
	v_exp_f32_e32 v44, v44
	v_exp_f32_e32 v45, v45
	v_exp_f32_e64 v46, v46
	v_exp_f32_e32 v47, v47
	s_waitcnt vmcnt(2) lgkmcnt(0)
	v_sub_f32_e32 v80, v64, v202
	v_sub_f32_e32 v81, v65, v202
	v_sub_f32_e32 v64, v82, v202
	v_sub_f32_e32 v65, v83, v202
	v_sub_f32_e32 v82, v66, v202
	v_sub_f32_e32 v83, v67, v202
	v_sub_f32_e32 v66, v84, v202
	v_sub_f32_e32 v67, v85, v202
	v_sub_f32_e32 v84, v68, v202
	v_sub_f32_e32 v85, v69, v202
	v_sub_f32_e32 v68, v86, v202
	v_sub_f32_e32 v69, v87, v202
	v_sub_f32_e32 v86, v70, v202
	v_sub_f32_e32 v87, v71, v202
	v_sub_f32_e32 v70, v88, v202
	v_sub_f32_e32 v71, v89, v202
	v_sub_f32_e32 v88, v72, v202
	v_sub_f32_e32 v89, v73, v202
	v_sub_f32_e32 v72, v90, v202
	v_sub_f32_e32 v73, v91, v202
	v_sub_f32_e32 v90, v74, v202
	v_sub_f32_e32 v91, v75, v202
	v_sub_f32_e32 v74, v92, v202
	v_sub_f32_e32 v75, v93, v202
	v_sub_f32_e32 v92, v76, v202
	v_sub_f32_e32 v93, v77, v202
	v_sub_f32_e32 v76, v138, v202
	v_sub_f32_e32 v77, v139, v202
	v_sub_f32_e32 v94, v78, v202
	v_sub_f32_e32 v95, v79, v202
	v_sub_f32_e32 v78, v140, v202
	v_sub_f32_e32 v79, v141, v202
	s_barrier
	s_andn2_b64 vcc, exec, s[18:19]
	s_cbranch_vccnz .LBB0_729
	s_waitcnt lgkmcnt(0)
	ds_read_b128 v[162:165], v219 offset:49248
	ds_read_b128 v[170:173], v219 offset:49216
	ds_read_b128 v[174:177], v219 offset:49184
	ds_read_b128 v[178:181], v219 offset:49152
	s_waitcnt lgkmcnt(3)
	s_nop 0
	v_pk_mul_f32 v[30:31], v[30:31], v[164:165]
	s_waitcnt lgkmcnt(2)
	s_nop 0
	v_pk_mul_f32 v[26:27], v[26:27], v[172:173]
	s_waitcnt lgkmcnt(1)
	s_nop 0
	v_pk_mul_f32 v[22:23], v[22:23], v[176:177]
	s_waitcnt lgkmcnt(0)
	s_nop 0
	v_pk_mul_f32 v[18:19], v[18:19], v[180:181]
	v_pk_mul_f32 v[28:29], v[28:29], v[162:163]
	v_pk_mul_f32 v[24:25], v[24:25], v[170:171]
	v_pk_mul_f32 v[20:21], v[20:21], v[174:175]
	v_pk_mul_f32 v[16:17], v[16:17], v[178:179]
	v_pk_mul_f32 v[14:15], v[14:15], v[164:165]
	v_pk_mul_f32 v[10:11], v[10:11], v[172:173]
	v_pk_mul_f32 v[6:7], v[6:7], v[176:177]
	v_pk_mul_f32 v[2:3], v[2:3], v[180:181]
	v_pk_mul_f32 v[12:13], v[12:13], v[162:163]
	v_pk_mul_f32 v[8:9], v[8:9], v[170:171]
	v_pk_mul_f32 v[4:5], v[4:5], v[174:175]
	v_pk_mul_f32 v[0:1], v[0:1], v[178:179]

.LBB0_730:
	v_mfma_f32_32x32x16_bf16 v[16:31], v[126:129], v[194:197], v[16:31]
	v_exp_f32_e32 v80, v80
	v_exp_f32_e32 v81, v81
	v_exp_f32_e64 v82, v82
	v_exp_f32_e32 v83, v83
	s_waitcnt lgkmcnt(14)
	v_mfma_f32_32x32x16_bf16 v[0:15], v[126:129], v[190:193], v[0:15]
	v_exp_f32_e32 v84, v84
	v_exp_f32_e32 v85, v85
	v_exp_f32_e32 v86, v86
	v_exp_f32_e32 v87, v87
	v_add_u32_e64 v48, s38, v238
	ds_read_b128 v[158:161], v48
	ds_read_b128 v[146:149], v48 offset:512
	v_mfma_f32_32x32x16_bf16 v[16:31], v[122:125], v[186:189], v[16:31]
	v_exp_f32_e32 v88, v88
	v_exp_f32_e32 v89, v89
	v_exp_f32_e32 v90, v90
	v_exp_f32_e32 v91, v91
	ds_read_b128 v[154:157], v48 offset:2048
	ds_read_b128 v[142:145], v48 offset:2560
	v_mfma_f32_32x32x16_bf16 v[0:15], v[122:125], v[138:141], v[0:15]
	v_exp_f32_e32 v92, v92
	v_exp_f32_e32 v93, v93
	v_exp_f32_e32 v94, v94
	v_exp_f32_e32 v95, v95
	ds_read_b128 v[150:153], v48 offset:4096
	ds_read_b128 v[138:141], v48 offset:4608
	v_mfma_f32_32x32x16_bf16 v[16:31], v[118:121], v[182:185], v[16:31]
	v_exp_f32_e32 v64, v64
	v_exp_f32_e32 v65, v65
	v_exp_f32_e32 v66, v66
	v_exp_f32_e32 v67, v67
	ds_read_b128 v[134:137], v48 offset:6144
	ds_read_b128 v[130:133], v48 offset:6656
	s_waitcnt lgkmcnt(14)
	s_nop 0
	v_mfma_f32_32x32x16_bf16 v[0:15], v[118:121], v[178:181], v[0:15]
	v_exp_f32_e32 v68, v68
	v_exp_f32_e32 v69, v69
	v_exp_f32_e32 v70, v70
	v_exp_f32_e32 v71, v71
	v_mfma_f32_32x32x16_bf16 v[16:31], v[114:117], v[174:177], v[16:31]
	v_exp_f32_e32 v72, v72
	v_exp_f32_e32 v73, v73
	v_exp_f32_e32 v74, v74
	v_exp_f32_e32 v75, v75
	v_mfma_f32_32x32x16_bf16 v[0:15], v[114:117], v[170:173], v[0:15]
	v_exp_f32_e32 v76, v76
	v_exp_f32_e32 v77, v77
	v_exp_f32_e64 v78, v78
	v_exp_f32_e32 v79, v79
	s_waitcnt vmcnt(2) lgkmcnt(0)
	v_sub_f32_e32 v48, v32, v202
	v_sub_f32_e32 v49, v33, v202
	v_sub_f32_e32 v32, v50, v202
	v_sub_f32_e32 v33, v51, v202
	v_sub_f32_e32 v50, v34, v202
	v_sub_f32_e32 v51, v35, v202
	v_sub_f32_e32 v34, v52, v202
	v_sub_f32_e32 v35, v53, v202
	v_sub_f32_e32 v52, v36, v202
	v_sub_f32_e32 v53, v37, v202
	v_sub_f32_e32 v36, v54, v202
	v_sub_f32_e32 v37, v55, v202
	v_sub_f32_e32 v54, v38, v202
	v_sub_f32_e32 v55, v39, v202
	v_sub_f32_e32 v38, v56, v202
	v_sub_f32_e32 v39, v57, v202
	v_sub_f32_e32 v56, v40, v202
	v_sub_f32_e32 v57, v41, v202
	v_sub_f32_e32 v40, v58, v202
	v_sub_f32_e32 v41, v59, v202
	v_sub_f32_e32 v58, v42, v202
	v_sub_f32_e32 v59, v43, v202
	v_sub_f32_e32 v42, v60, v202
	v_sub_f32_e32 v43, v61, v202
	v_sub_f32_e32 v60, v44, v202
	v_sub_f32_e32 v61, v45, v202
	v_sub_f32_e32 v44, v162, v202
	v_sub_f32_e32 v45, v163, v202
	v_sub_f32_e32 v62, v46, v202
	v_sub_f32_e32 v63, v47, v202
	v_sub_f32_e32 v46, v164, v202
	v_sub_f32_e32 v47, v165, v202
	s_barrier
	s_andn2_b64 vcc, exec, s[18:19]
	s_cbranch_vccnz .LBB0_732
	s_waitcnt lgkmcnt(0)
	ds_read_b128 v[166:169], v219 offset:49248
	ds_read_b128 v[170:173], v219 offset:49216
	ds_read_b128 v[174:177], v219 offset:49184
	ds_read_b128 v[178:181], v219 offset:49152
	s_waitcnt lgkmcnt(3)
	s_nop 0
	v_pk_mul_f32 v[30:31], v[30:31], v[168:169]
	s_waitcnt lgkmcnt(2)
	s_nop 0
	v_pk_mul_f32 v[26:27], v[26:27], v[172:173]
	s_waitcnt lgkmcnt(1)
	s_nop 0
	v_pk_mul_f32 v[22:23], v[22:23], v[176:177]
	s_waitcnt lgkmcnt(0)
	s_nop 0
	v_pk_mul_f32 v[18:19], v[18:19], v[180:181]
	v_pk_mul_f32 v[28:29], v[28:29], v[166:167]
	v_pk_mul_f32 v[24:25], v[24:25], v[170:171]
	v_pk_mul_f32 v[20:21], v[20:21], v[174:175]
	v_pk_mul_f32 v[16:17], v[16:17], v[178:179]
	v_pk_mul_f32 v[14:15], v[14:15], v[168:169]
	v_pk_mul_f32 v[10:11], v[10:11], v[172:173]
	v_pk_mul_f32 v[6:7], v[6:7], v[176:177]
	v_pk_mul_f32 v[2:3], v[2:3], v[180:181]
	v_pk_mul_f32 v[12:13], v[12:13], v[166:167]
	v_pk_mul_f32 v[8:9], v[8:9], v[170:171]
	v_pk_mul_f32 v[4:5], v[4:5], v[174:175]
	v_pk_mul_f32 v[0:1], v[0:1], v[178:179]
